# sel block pairing: proposal window narrowed to +-4 list positions (keeps the blocks of a triple closer in memory), three rounds
# speedup vs baseline: 1.0051x; 1.0051x over previous
; #define LAS __attribute__((address_space(3)))
; template <bool DUMMY> __device__ __forceinline__ void sel_phase(Frame& F) {
;     const bf16* Q = (const bf16*)(F.ws + SC_Q); const char* KS = (const char*)(F.ws + SC_KV + 2 * KVS);        const char* VS = (const char*)(F.ws + SC_KV + 1 * KVS);
;     bf16* OW = (bf16*)(F.ws + SC_OW); const float* gates = (const float*)(F.ws + SM_GATES); const unsigned long long* SELM = (const unsigned long long*)(F.ws + SM_SELM);
;     const int lane = F.lane, c = lane & 15, kq = lane >> 4;
;     LAS unsigned long long* Ml = (LAS unsigned long long*)(F.lds + RING_ML_OFF);
;     LAS unsigned short* Lst = (LAS unsigned short*)(F.lds + RING_LIST_OFF); LAS unsigned* Wc = (LAS unsigned*)(F.lds + RING_LIST_OFF + 512);
;     LAS u32x2* PD = (LAS u32x2*)(F.lds + 6 * SLOTS);
;     const int vtlane = c * VT8ST + 8 * kq; const int klane = c * K8ST + 32 * kq;
;     RingSLane RL; ringS_lane_init(RL, F.wave, lane);
;     ...
;             const int ia = F.tid >> 2, sub = F.tid & 3;
; #pragma unroll 1
;             for (int r = 0; r < 3 && nB > 0; ++r) {
;                 if (F.tid < 128) PRP[F.tid] = 0xffffffffu;
;                 __syncthreads();
;                 const bool va = ia < npair && PB[ia] == (unsigned short)0xffffu; unsigned best = 0xffffffffu;
;                 if (va) { const unsigned pa = PW[ia]; const int klo = ia - 8 > 0 ? ia - 8 : 0, khi = ia + 8 < nB - 1 ? ia + 8 : nB - 1;
;                     for (int k = klo + sub; k <= khi; k += 4) if (MB[k] == 0) { const unsigned x = pa + PW[npair + k];
.LBB0_1699:
	s_cmpk_gt_i32 s77, 0x7ff
	s_cbranch_scc1 .LBB0_1817
	s_add_u32 s22, s28, 0x1a000000
	s_addc_u32 s23, s29, 0
	s_add_u32 s78, s28, 0x26000000
	s_addc_u32 s79, s29, 0
	s_add_u32 s80, s28, 0x24000000
	s_addc_u32 s81, s29, 0
	s_add_u32 s24, s28, 0x2e000000
	v_writelane_b32 v238, s90, 7
	s_addc_u32 s25, s29, 0
	v_add_u32_e32 v0, s8, v0
	v_writelane_b32 v238, s92, 3
	s_add_u32 s42, s28, 0xe40000
	v_add_u32_e32 v0, 0x4000, v0
	s_mov_b32 s2, 0x66666667
	v_writelane_b32 v238, s93, 4
	s_addc_u32 s43, s29, 0
	v_mul_hi_i32 v1, v0, s2
	s_lshl_b32 s83, s96, 3
	v_writelane_b32 v238, s94, 5
	v_lshrrev_b32_e32 v9, 31, v1
	v_ashrrev_i32_e32 v1, 5, v1
	s_cmpk_gt_u32 s21, 0xff
	v_writelane_b32 v238, s95, 6
	v_add_u32_e32 v1, v1, v9
	s_movk_i32 s10, 0x50
	s_cselect_b64 s[4:5], -1, 0
	v_min_i32_e32 v9, 0x7f, v1
	v_mul_lo_u32 v1, v1, s10
	v_writelane_b32 v238, s4, 8
	s_cmpk_lt_u32 s21, 0x100
	v_sub_u32_e32 v0, v0, v1
	v_cmp_eq_u32_e32 vcc, 0, v2
	v_writelane_b32 v238, s5, 9
	s_cselect_b64 s[4:5], -1, 0
	v_ashrrev_i32_e32 v0, 4, v0
	s_and_b64 s[46:47], s[4:5], vcc
	v_lshlrev_b32_e32 v9, 6, v9
	v_min_i32_e32 v0, 3, v0
	s_bitcmp1_b32 s21, 6
	v_lshl_add_u32 v108, v0, 4, v9
	v_lshlrev_b64 v[0:1], v2, -1
	s_cselect_b64 s[48:49], -1, 0
	s_add_i32 s84, s83, 0
	v_not_b32_e32 v110, v0
	s_movk_i32 s6, 0x80
	v_and_b32_e32 v0, 0xffffff80, v100
	s_add_i32 s84, s84, 0x1c800
	s_add_i32 s85, s8, 0
	v_ashrrev_i32_e32 v101, 31, v100
	v_not_b32_e32 v111, v1
	v_cmp_gt_i32_e64 s[4:5], s6, v100
	v_cmp_eq_u32_e64 s[6:7], s6, v0
	s_cmpk_lt_u32 s21, 0xc0
	v_lshl_add_u64 v[0:1], v[100:101], 3, s[28:29]
	s_mov_b64 s[8:9], 0x1450000
	s_cselect_b64 s[50:51], -1, 0
	v_lshl_add_u64 v[112:113], v[0:1], 0, s[8:9]
	s_add_i32 s8, 0, 0x23000
	v_lshl_add_u32 v101, v100, 3, s8
	s_lshl_b32 s8, s96, 2
	s_add_i32 s88, s8, 0
	v_lshlrev_b32_e32 v0, 1, v100
	s_add_i32 s8, 0, 0x23800
	v_add_u32_e32 v157, s8, v0
	v_lshlrev_b32_e32 v1, 2, v100
	s_add_i32 s8, 0, 0x1a400
	s_add_i32 s12, 0, 0x1a800
	v_ashrrev_i32_e32 v156, 2, v100
	v_add_u32_e32 v158, s8, v1
	s_add_i32 s11, 0, 0x1aa00
	v_add_u32_e32 v165, s12, v1
	v_and_b32_e32 v1, 0x7f, v100
	v_add_u32_e32 v159, s11, v0
	v_lshl_add_u32 v160, v156, 1, s11
	v_lshl_add_u32 v166, v1, 1, s11
	s_add_i32 s11, 0, 0x1ab80
	s_add_i32 s21, s88, 0x23a00
	s_add_i32 s87, s88, 0x1ac80
	s_add_i32 s88, s88, 0x1ac7c
	v_add_u32_e32 v169, s11, v0
	s_add_i32 s11, 0, 0x1ac90
	s_add_u32 s52, s28, 0x3b400000
	v_add_u32_e32 v170, s11, v0
	s_addc_u32 s53, s29, 0
	s_add_i32 s11, s96, -4
	s_lshr_b32 s12, s11, 2
	s_add_i32 s12, s12, 1
	s_and_b32 s34, s96, 0x3fffffc
	s_and_b32 s13, s12, 7
	s_cmp_gt_u32 s11, 27
	s_cselect_b64 s[36:37], -1, 0
	v_writelane_b32 v238, s36, 10
	s_and_b32 s11, s12, 0x7ffffff8
	s_cmp_lg_u32 s13, 0
	v_writelane_b32 v238, s37, 11
	v_writelane_b32 v238, s11, 12
	s_cselect_b64 s[36:37], -1, 0
	v_writelane_b32 v238, s36, 13
	s_cmp_lg_u32 s96, s34
	v_lshl_add_u32 v102, v3, 4, v4
	v_writelane_b32 v238, s37, 14
	v_ashrrev_i32_e32 v4, 4, v2
	v_writelane_b32 v238, s34, 15
	s_cselect_b64 s[34:35], -1, 0
	v_lshlrev_b32_e32 v7, 3, v4
	v_lshlrev_b32_e32 v104, 5, v4
	v_lshlrev_b32_e32 v155, 2, v4
	v_and_b32_e32 v4, -4, v100
	v_writelane_b32 v238, s34, 16
	v_and_b32_e32 v3, 15, v2
	v_and_b32_e32 v153, 3, v2
	v_add_u32_e32 v161, s8, v4
	v_max_i32_e32 v4, 4, v156
	v_writelane_b32 v238, s35, 17
	s_lshl_b32 s11, s13, 4
	v_lshlrev_b32_e32 v0, 3, v2
	v_mul_u32_u24_e32 v8, 0x90, v3
	v_bfe_u32 v152, v2, 2, 2
	v_mov_b32_e32 v17, 0
	s_movk_i32 s2, 0x100
	v_add_u32_e32 v163, v4, v153
	v_writelane_b32 v238, s11, 18
	v_lshl_add_u32 v172, s96, 9, v0
	v_mad_u32_u24 v0, v3, s10, 0
	s_movk_i32 s10, 0x2400
	v_lshl_add_u32 v106, v5, 4, v6
	v_ashrrev_i32_e32 v105, 31, v104
	s_mov_b32 s82, 0
	v_mov_b32_e32 v103, v17
	v_mov_b32_e32 v107, v17
	v_mov_b32_e32 v109, v17
	v_lshlrev_b32_e64 v154, v152, 1
	v_cmp_gt_i32_e64 s[2:3], s2, v100
	s_movk_i32 s86, 0xc0
	v_add_u32_e32 v162, 4, v156
	v_add_u32_e32 v164, -4, v163
	v_cmp_eq_u32_e64 s[8:9], 0, v153
	v_add_u32_e32 v167, 0xffffff80, v100
	v_add_u16_e32 v168, 0xff80, v100
	v_sub_u32_e32 v171, 0, v156
	v_writelane_b32 v238, s96, 19
	v_add3_u32 v173, v0, v7, s10
	v_add_u32_e32 v173, v173, v7
	v_add3_u32 v174, v8, 0, v104
	v_mov_b32_e32 v175, -1
	v_mov_b32_e32 v176, 1
	s_add_i32 s92, 0, 0x1ac88
	s_mov_b32 s93, 0xffff
	s_add_i32 s94, s85, 0x2000
	s_add_i32 s95, s85, 0x4c00
	s_add_i32 s96, s85, 0x6c00
	s_add_i32 s10, s85, 0x8c00
	s_add_i32 s34, s85, 0x9800
	s_add_i32 s35, s85, 0xb800
	s_add_i32 s75, s85, 0xd800
	s_mov_b32 s90, 0xefa18f08
	v_mov_b32_e32 v177, 0x7c7c7c7c
	v_mov_b32_e32 v178, 0x7f7f7f7f
	s_brev_b32 s91, -3
	v_mov_b32_e32 v115, 0x40400000
	v_mov_b32_e32 v179, 0x1a3e0
	v_mov_b32_e32 v180, 0x1000000
	v_mov_b32_e32 v181, 0xff800000
	s_mov_b32 s74, s77
	v_writelane_b32 v238, s10, 20
	s_branch .LBB0_1703
